# nt hint on the riders' once-read fp32 W_u loads
# speedup vs baseline: 1.0169x; 1.0009x over previous
_Z16gemm_glds_kernelILi2EEvPKDF16_PDF16_PKiS4_S1_S1_PKfiS6_Pc:
	s_load_dword s3, s[0:1], 0x38
	s_mov_b64 s[4:5], -1
	s_waitcnt lgkmcnt(0)
	s_cmp_lt_i32 s2, s3
	s_cbranch_scc1 .LBB2_2
	s_sub_i32 s3, s2, s3
	s_cmp_gt_u32 s3, 255
	s_cbranch_scc1 .LBB2_14
	s_load_dwordx4 s[4:7], s[0:1], 0x40
	v_lshrrev_b32_e32 v1, 8, v0
	v_and_b32_e32 v2, 0xff, v0
	v_and_b32_e32 v3, 63, v0
	v_readfirstlane_b32 s8, v1
	v_bfe_u32 v4, v0, 6, 2
	s_lshl_b32 s9, s3, 1
	s_nop 1
	s_add_u32 s9, s9, s8
	s_lshr_b32 s10, s9, 8
	s_bfe_u32 s11, s9, 0x40004
	s_and_b32 s12, s9, 15
	s_lshl_b32 s13, s11, 6
	s_lshl_b32 s14, s12, 6
	s_mul_i32 s15, s10, 0x3d2844
	s_movk_i32 s24, 0x3e9
	s_waitcnt lgkmcnt(0)
	s_add_u32 s16, s4, s15
	s_addc_u32 s17, s5, 0
	s_add_u32 s18, s16, 0x7a5088
	s_addc_u32 s19, s17, 0
	s_lshl_b32 s15, s10, 21
	s_add_u32 s20, s6, s15
	s_addc_u32 s21, s7, 0
	s_add_u32 s20, s20, 0x800000
	s_addc_u32 s21, s21, 0
	s_add_u32 s22, s20, 0x400000
	s_addc_u32 s23, s21, 0
	v_add_u32_e32 v5, s13, v4
	v_add_u32_e32 v6, s14, v3
	v_cmp_gt_u32_e64 s[28:29], s24, v6
	v_min_u32_e32 v6, 0x3e8, v6
	v_lshlrev_b32_e32 v6, 2, v6
	v_min_u32_e32 v7, 0x3e8, v5
	v_mul_u32_u24_e32 v7, 0xfa4, v7
	v_add_u32_e32 v48, v7, v6
	v_add_u32_e32 v7, 4, v5
	v_min_u32_e32 v7, 0x3e8, v7
	v_mul_u32_u24_e32 v7, 0xfa4, v7
	v_add_u32_e32 v49, v7, v6
	v_add_u32_e32 v7, 8, v5
	v_min_u32_e32 v7, 0x3e8, v7
	v_mul_u32_u24_e32 v7, 0xfa4, v7
	v_add_u32_e32 v50, v7, v6
	v_add_u32_e32 v7, 12, v5
	v_min_u32_e32 v7, 0x3e8, v7
	v_mul_u32_u24_e32 v7, 0xfa4, v7
	v_add_u32_e32 v51, v7, v6
	v_add_u32_e32 v7, 16, v5
	v_min_u32_e32 v7, 0x3e8, v7
	v_mul_u32_u24_e32 v7, 0xfa4, v7
	v_add_u32_e32 v52, v7, v6
	v_add_u32_e32 v7, 20, v5
	v_min_u32_e32 v7, 0x3e8, v7
	v_mul_u32_u24_e32 v7, 0xfa4, v7
	v_add_u32_e32 v53, v7, v6
	v_add_u32_e32 v7, 24, v5
	v_min_u32_e32 v7, 0x3e8, v7
	v_mul_u32_u24_e32 v7, 0xfa4, v7
	v_add_u32_e32 v54, v7, v6
	v_add_u32_e32 v7, 28, v5
	v_min_u32_e32 v7, 0x3e8, v7
	v_mul_u32_u24_e32 v7, 0xfa4, v7
	v_add_u32_e32 v55, v7, v6
	v_add_u32_e32 v7, 32, v5
	v_min_u32_e32 v7, 0x3e8, v7
	v_mul_u32_u24_e32 v7, 0xfa4, v7
	v_add_u32_e32 v56, v7, v6
	v_add_u32_e32 v7, 36, v5
	v_min_u32_e32 v7, 0x3e8, v7
	v_mul_u32_u24_e32 v7, 0xfa4, v7
	v_add_u32_e32 v57, v7, v6
	v_add_u32_e32 v7, 40, v5
	v_min_u32_e32 v7, 0x3e8, v7
	v_mul_u32_u24_e32 v7, 0xfa4, v7
	v_add_u32_e32 v58, v7, v6
	v_add_u32_e32 v7, 44, v5
	v_min_u32_e32 v7, 0x3e8, v7
	v_mul_u32_u24_e32 v7, 0xfa4, v7
	v_add_u32_e32 v59, v7, v6
	v_add_u32_e32 v7, 48, v5
	v_min_u32_e32 v7, 0x3e8, v7
	v_mul_u32_u24_e32 v7, 0xfa4, v7
	v_add_u32_e32 v60, v7, v6
	v_add_u32_e32 v7, 52, v5
	v_min_u32_e32 v7, 0x3e8, v7
	v_mul_u32_u24_e32 v7, 0xfa4, v7
	v_add_u32_e32 v61, v7, v6
	v_add_u32_e32 v7, 56, v5
	v_min_u32_e32 v7, 0x3e8, v7
	v_mul_u32_u24_e32 v7, 0xfa4, v7
	v_add_u32_e32 v62, v7, v6
	v_add_u32_e32 v7, 60, v5
	v_min_u32_e32 v7, 0x3e8, v7
	v_mul_u32_u24_e32 v7, 0xfa4, v7
	v_add_u32_e32 v63, v7, v6
	global_load_dword v16, v48, s[16:17] nt
	global_load_dword v17, v49, s[16:17] nt
	global_load_dword v18, v50, s[16:17] nt
	global_load_dword v19, v51, s[16:17] nt
	global_load_dword v20, v52, s[16:17] nt
	global_load_dword v21, v53, s[16:17] nt
	global_load_dword v22, v54, s[16:17] nt
	global_load_dword v23, v55, s[16:17] nt
	global_load_dword v24, v56, s[16:17] nt
	global_load_dword v25, v57, s[16:17] nt
	global_load_dword v26, v58, s[16:17] nt
	global_load_dword v27, v59, s[16:17] nt
	global_load_dword v28, v60, s[16:17] nt
	global_load_dword v29, v61, s[16:17] nt
	global_load_dword v30, v62, s[16:17] nt
	global_load_dword v31, v63, s[16:17] nt
	global_load_dword v32, v48, s[18:19] nt
	global_load_dword v33, v49, s[18:19] nt
	global_load_dword v34, v50, s[18:19] nt
	global_load_dword v35, v51, s[18:19] nt
	global_load_dword v36, v52, s[18:19] nt
	global_load_dword v37, v53, s[18:19] nt
	global_load_dword v38, v54, s[18:19] nt
	global_load_dword v39, v55, s[18:19] nt
	global_load_dword v40, v56, s[18:19] nt
	global_load_dword v41, v57, s[18:19] nt
	global_load_dword v42, v58, s[18:19] nt
	global_load_dword v43, v59, s[18:19] nt
	global_load_dword v44, v60, s[18:19] nt
	global_load_dword v45, v61, s[18:19] nt
	global_load_dword v46, v62, s[18:19] nt
	global_load_dword v47, v63, s[18:19] nt
	v_mul_u32_u24_e32 v8, 65, v4
	v_add_u32_e32 v8, v8, v3
	v_lshlrev_b32_e32 v8, 2, v8
	s_mul_i32 s25, s8, 0x4100
	v_add_u32_e32 v8, s25, v8
	v_and_b32_e32 v9, 7, v2
	v_lshrrev_b32_e32 v10, 3, v2
	v_mul_u32_u24_e32 v11, 0x208, v9
	v_add_u32_e32 v11, v11, v10
	v_lshlrev_b32_e32 v11, 2, v11
	v_add_u32_e32 v11, s25, v11
	v_add_u32_e32 v12, s14, v10
	v_lshlrev_b32_e32 v12, 11, v12
	v_lshlrev_b32_e32 v13, 4, v9
	v_add_u32_e32 v12, v12, v13
	s_lshl_b32 s26, s13, 1
	v_add_u32_e32 v12, s26, v12
	v_add_u32_e32 v14, 0x10000, v12
	s_waitcnt vmcnt(31)
	v_cmp_gt_u32_e32 vcc, s24, v5
	s_and_b64 vcc, vcc, s[28:29]
	s_nop 1
	v_cndmask_b32_e32 v7, 0, v16, vcc
	ds_write_b32 v8, v7
	s_waitcnt vmcnt(30)
	v_add_u32_e32 v7, 4, v5
	v_cmp_gt_u32_e32 vcc, s24, v7
	s_and_b64 vcc, vcc, s[28:29]
	s_nop 1
	v_cndmask_b32_e32 v7, 0, v17, vcc
	ds_write_b32 v8, v7 offset:1040
	s_waitcnt vmcnt(29)
	v_add_u32_e32 v7, 8, v5
	v_cmp_gt_u32_e32 vcc, s24, v7
	s_and_b64 vcc, vcc, s[28:29]
	s_nop 1
	v_cndmask_b32_e32 v7, 0, v18, vcc
	ds_write_b32 v8, v7 offset:2080
	s_waitcnt vmcnt(28)
	v_add_u32_e32 v7, 12, v5
	v_cmp_gt_u32_e32 vcc, s24, v7
	s_and_b64 vcc, vcc, s[28:29]
	s_nop 1
	v_cndmask_b32_e32 v7, 0, v19, vcc
	ds_write_b32 v8, v7 offset:3120
	s_waitcnt vmcnt(27)
	v_add_u32_e32 v7, 16, v5
	v_cmp_gt_u32_e32 vcc, s24, v7
	s_and_b64 vcc, vcc, s[28:29]
	s_nop 1
	v_cndmask_b32_e32 v7, 0, v20, vcc
	ds_write_b32 v8, v7 offset:4160
	s_waitcnt vmcnt(26)
	v_add_u32_e32 v7, 20, v5
	v_cmp_gt_u32_e32 vcc, s24, v7
	s_and_b64 vcc, vcc, s[28:29]
	s_nop 1
	v_cndmask_b32_e32 v7, 0, v21, vcc
	ds_write_b32 v8, v7 offset:5200
	s_waitcnt vmcnt(25)
	v_add_u32_e32 v7, 24, v5
	v_cmp_gt_u32_e32 vcc, s24, v7
	s_and_b64 vcc, vcc, s[28:29]
	s_nop 1
	v_cndmask_b32_e32 v7, 0, v22, vcc
	ds_write_b32 v8, v7 offset:6240
	s_waitcnt vmcnt(24)
	v_add_u32_e32 v7, 28, v5
	v_cmp_gt_u32_e32 vcc, s24, v7
	s_and_b64 vcc, vcc, s[28:29]
	s_nop 1
	v_cndmask_b32_e32 v7, 0, v23, vcc
	ds_write_b32 v8, v7 offset:7280
	s_waitcnt vmcnt(23)
	v_add_u32_e32 v7, 32, v5
	v_cmp_gt_u32_e32 vcc, s24, v7
	s_and_b64 vcc, vcc, s[28:29]
	s_nop 1
	v_cndmask_b32_e32 v7, 0, v24, vcc
	ds_write_b32 v8, v7 offset:8320
	s_waitcnt vmcnt(22)
	v_add_u32_e32 v7, 36, v5
	v_cmp_gt_u32_e32 vcc, s24, v7
	s_and_b64 vcc, vcc, s[28:29]
	s_nop 1
	v_cndmask_b32_e32 v7, 0, v25, vcc
	ds_write_b32 v8, v7 offset:9360
	s_waitcnt vmcnt(21)
	v_add_u32_e32 v7, 40, v5
	v_cmp_gt_u32_e32 vcc, s24, v7
	s_and_b64 vcc, vcc, s[28:29]
	s_nop 1
	v_cndmask_b32_e32 v7, 0, v26, vcc
	ds_write_b32 v8, v7 offset:10400
	s_waitcnt vmcnt(20)
	v_add_u32_e32 v7, 44, v5
	v_cmp_gt_u32_e32 vcc, s24, v7
	s_and_b64 vcc, vcc, s[28:29]
	s_nop 1
	v_cndmask_b32_e32 v7, 0, v27, vcc
	ds_write_b32 v8, v7 offset:11440
	s_waitcnt vmcnt(19)
	v_add_u32_e32 v7, 48, v5
	v_cmp_gt_u32_e32 vcc, s24, v7
	s_and_b64 vcc, vcc, s[28:29]
	s_nop 1
	v_cndmask_b32_e32 v7, 0, v28, vcc
	ds_write_b32 v8, v7 offset:12480
	s_waitcnt vmcnt(18)
	v_add_u32_e32 v7, 52, v5
	v_cmp_gt_u32_e32 vcc, s24, v7
	s_and_b64 vcc, vcc, s[28:29]
	s_nop 1
	v_cndmask_b32_e32 v7, 0, v29, vcc
	ds_write_b32 v8, v7 offset:13520
	s_waitcnt vmcnt(17)
	v_add_u32_e32 v7, 56, v5
	v_cmp_gt_u32_e32 vcc, s24, v7
	s_and_b64 vcc, vcc, s[28:29]
	s_nop 1
	v_cndmask_b32_e32 v7, 0, v30, vcc
	ds_write_b32 v8, v7 offset:14560
	s_waitcnt vmcnt(16)
	v_add_u32_e32 v7, 60, v5
	v_cmp_gt_u32_e32 vcc, s24, v7
	s_and_b64 vcc, vcc, s[28:29]
	s_nop 1
	v_cndmask_b32_e32 v7, 0, v31, vcc
	ds_write_b32 v8, v7 offset:15600
	s_waitcnt lgkmcnt(0)
	s_barrier
	ds_read_b32 v64, v11
	ds_read_b32 v65, v11 offset:260
	ds_read_b32 v66, v11 offset:520
	ds_read_b32 v67, v11 offset:780
	ds_read_b32 v68, v11 offset:1040
	ds_read_b32 v69, v11 offset:1300
	ds_read_b32 v70, v11 offset:1560
	ds_read_b32 v71, v11 offset:1820
	ds_read_b32 v72, v11 offset:128
	ds_read_b32 v73, v11 offset:388
	ds_read_b32 v74, v11 offset:648
	ds_read_b32 v75, v11 offset:908
	s_waitcnt lgkmcnt(4)
	ds_read_b32 v76, v11 offset:1168
	ds_read_b32 v77, v11 offset:1428
	ds_read_b32 v78, v11 offset:1688
	ds_read_b32 v79, v11 offset:1948
	s_waitcnt lgkmcnt(0)
	v_cvt_pk_f16_f32 v80, v64, v65
	v_cvt_pk_f16_f32 v81, v66, v67
	v_cvt_pk_f16_f32 v82, v68, v69
	v_cvt_pk_f16_f32 v83, v70, v71
	v_cvt_pk_f16_f32 v84, v72, v73
	v_cvt_pk_f16_f32 v85, v74, v75
	v_cvt_pk_f16_f32 v86, v76, v77
	v_cvt_pk_f16_f32 v87, v78, v79
	global_store_dwordx4 v12, v[80:83], s[20:21]
	global_store_dwordx4 v14, v[84:87], s[20:21]
	s_barrier
	s_waitcnt vmcnt(17)
	v_cmp_gt_u32_e32 vcc, s24, v5
	s_and_b64 vcc, vcc, s[28:29]
	s_nop 1
	v_cndmask_b32_e32 v7, 0, v32, vcc
	ds_write_b32 v8, v7
	s_waitcnt vmcnt(16)
	v_add_u32_e32 v7, 4, v5
	v_cmp_gt_u32_e32 vcc, s24, v7
	s_and_b64 vcc, vcc, s[28:29]
	s_nop 1
	v_cndmask_b32_e32 v7, 0, v33, vcc
	ds_write_b32 v8, v7 offset:1040
	s_waitcnt vmcnt(15)
	v_add_u32_e32 v7, 8, v5
	v_cmp_gt_u32_e32 vcc, s24, v7
	s_and_b64 vcc, vcc, s[28:29]
	s_nop 1
	v_cndmask_b32_e32 v7, 0, v34, vcc
	ds_write_b32 v8, v7 offset:2080
	s_waitcnt vmcnt(14)
	v_add_u32_e32 v7, 12, v5
	v_cmp_gt_u32_e32 vcc, s24, v7
	s_and_b64 vcc, vcc, s[28:29]
	s_nop 1
	v_cndmask_b32_e32 v7, 0, v35, vcc
	ds_write_b32 v8, v7 offset:3120
	s_waitcnt vmcnt(13)
	v_add_u32_e32 v7, 16, v5
	v_cmp_gt_u32_e32 vcc, s24, v7
	s_and_b64 vcc, vcc, s[28:29]
	s_nop 1
	v_cndmask_b32_e32 v7, 0, v36, vcc
	ds_write_b32 v8, v7 offset:4160
	s_waitcnt vmcnt(12)
	v_add_u32_e32 v7, 20, v5
	v_cmp_gt_u32_e32 vcc, s24, v7
	s_and_b64 vcc, vcc, s[28:29]
	s_nop 1
	v_cndmask_b32_e32 v7, 0, v37, vcc
	ds_write_b32 v8, v7 offset:5200
	s_waitcnt vmcnt(11)
	v_add_u32_e32 v7, 24, v5
	v_cmp_gt_u32_e32 vcc, s24, v7
	s_and_b64 vcc, vcc, s[28:29]
	s_nop 1
	v_cndmask_b32_e32 v7, 0, v38, vcc
	ds_write_b32 v8, v7 offset:6240
	s_waitcnt vmcnt(10)
	v_add_u32_e32 v7, 28, v5
	v_cmp_gt_u32_e32 vcc, s24, v7
	s_and_b64 vcc, vcc, s[28:29]
	s_nop 1
	v_cndmask_b32_e32 v7, 0, v39, vcc
	ds_write_b32 v8, v7 offset:7280
	s_waitcnt vmcnt(9)
	v_add_u32_e32 v7, 32, v5
	v_cmp_gt_u32_e32 vcc, s24, v7
	s_and_b64 vcc, vcc, s[28:29]
	s_nop 1
	v_cndmask_b32_e32 v7, 0, v40, vcc
	ds_write_b32 v8, v7 offset:8320
	s_waitcnt vmcnt(8)
	v_add_u32_e32 v7, 36, v5
	v_cmp_gt_u32_e32 vcc, s24, v7
	s_and_b64 vcc, vcc, s[28:29]
	s_nop 1
	v_cndmask_b32_e32 v7, 0, v41, vcc
	ds_write_b32 v8, v7 offset:9360
	s_waitcnt vmcnt(7)
	v_add_u32_e32 v7, 40, v5
	v_cmp_gt_u32_e32 vcc, s24, v7
	s_and_b64 vcc, vcc, s[28:29]
	s_nop 1
	v_cndmask_b32_e32 v7, 0, v42, vcc
	ds_write_b32 v8, v7 offset:10400
	s_waitcnt vmcnt(6)
	v_add_u32_e32 v7, 44, v5
	v_cmp_gt_u32_e32 vcc, s24, v7
	s_and_b64 vcc, vcc, s[28:29]
	s_nop 1
	v_cndmask_b32_e32 v7, 0, v43, vcc
	ds_write_b32 v8, v7 offset:11440
	s_waitcnt vmcnt(5)
	v_add_u32_e32 v7, 48, v5
	v_cmp_gt_u32_e32 vcc, s24, v7
	s_and_b64 vcc, vcc, s[28:29]
	s_nop 1
	v_cndmask_b32_e32 v7, 0, v44, vcc
	ds_write_b32 v8, v7 offset:12480
	s_waitcnt vmcnt(4)
	v_add_u32_e32 v7, 52, v5
	v_cmp_gt_u32_e32 vcc, s24, v7
	s_and_b64 vcc, vcc, s[28:29]
	s_nop 1
	v_cndmask_b32_e32 v7, 0, v45, vcc
	ds_write_b32 v8, v7 offset:13520
	s_waitcnt vmcnt(3)
	v_add_u32_e32 v7, 56, v5
	v_cmp_gt_u32_e32 vcc, s24, v7
	s_and_b64 vcc, vcc, s[28:29]
	s_nop 1
	v_cndmask_b32_e32 v7, 0, v46, vcc
	ds_write_b32 v8, v7 offset:14560
	s_waitcnt vmcnt(2)
	v_add_u32_e32 v7, 60, v5
	v_cmp_gt_u32_e32 vcc, s24, v7
	s_and_b64 vcc, vcc, s[28:29]
	s_nop 1
	v_cndmask_b32_e32 v7, 0, v47, vcc
	ds_write_b32 v8, v7 offset:15600
	s_waitcnt lgkmcnt(0)
	s_barrier
	ds_read_b32 v64, v11
	ds_read_b32 v65, v11 offset:260
	ds_read_b32 v66, v11 offset:520
	ds_read_b32 v67, v11 offset:780
	ds_read_b32 v68, v11 offset:1040
	ds_read_b32 v69, v11 offset:1300
	ds_read_b32 v70, v11 offset:1560
	ds_read_b32 v71, v11 offset:1820
	ds_read_b32 v72, v11 offset:128
	ds_read_b32 v73, v11 offset:388
	ds_read_b32 v74, v11 offset:648
	ds_read_b32 v75, v11 offset:908
	s_waitcnt lgkmcnt(4)
	ds_read_b32 v76, v11 offset:1168
	ds_read_b32 v77, v11 offset:1428
	ds_read_b32 v78, v11 offset:1688
	ds_read_b32 v79, v11 offset:1948
	s_waitcnt lgkmcnt(0)
	v_cvt_pk_f16_f32 v80, v64, v65
	v_cvt_pk_f16_f32 v81, v66, v67
	v_cvt_pk_f16_f32 v82, v68, v69
	v_cvt_pk_f16_f32 v83, v70, v71
	v_cvt_pk_f16_f32 v84, v72, v73
	v_cvt_pk_f16_f32 v85, v74, v75
	v_cvt_pk_f16_f32 v86, v76, v77
	v_cvt_pk_f16_f32 v87, v78, v79
	global_store_dwordx4 v12, v[80:83], s[22:23]
	global_store_dwordx4 v14, v[84:87], s[22:23]
	s_branch .LBB2_14
